# dilated-window attention unit epilogue: lane^16 exchange (v_permlane16_swap) + 8 global_store_dwordx4 per wave instead of 16 dwordx2
# speedup vs baseline: 1.0039x; 1.0039x over previous
.LBB0_406:
	v_and_b32_e32 v3, 64, v208
	v_xor_b32_e32 v1, 16, v208
	v_add_u32_e32 v3, 64, v3
	v_cmp_lt_i32_e32 vcc, v1, v3
	v_xor_b32_e32 v5, 32, v208
	s_mov_b32 s3, s15
	v_cndmask_b32_e32 v1, v208, v1, vcc
	v_lshlrev_b32_e32 v1, 2, v1
	ds_bpermute_b32 v4, v1, v152
	v_cmp_lt_i32_e32 vcc, v5, v3
	s_lshl_b64 s[0:1], s[2:3], 13
	s_lshl_b32 s38, s33, 7
	v_cndmask_b32_e32 v3, v208, v5, vcc
	v_lshlrev_b32_e32 v3, 2, v3
	s_waitcnt lgkmcnt(0)
	v_add_f32_e32 v4, v152, v4
	ds_bpermute_b32 v5, v3, v4
	v_ashrrev_i32_e32 v143, 31, v142
	s_waitcnt vmcnt(0) lgkmcnt(0)
	s_barrier
	s_waitcnt vmcnt(0) lgkmcnt(0)
	v_add_f32_e32 v38, v4, v5
	v_div_scale_f32 v4, s[2:3], v38, v38, 1.0
	v_rcp_f32_e32 v5, v4
	s_or_b64 s[2:3], s[0:1], s[14:15]
	s_lshl_b32 s14, s38, 1
	v_cmp_gt_u32_e64 s[0:1], 16, v179
	v_fma_f32 v39, -v4, v5, 1.0
	v_fmac_f32_e32 v5, v39, v5
	v_div_scale_f32 v39, vcc, 1.0, v38, 1.0
	v_mul_f32_e32 v40, v39, v5
	v_fma_f32 v41, -v4, v40, v39
	v_fmac_f32_e32 v40, v41, v5
	v_fma_f32 v4, -v4, v40, v39
	v_div_fmas_f32 v4, v4, v5, v40
	v_div_fixup_f32 v40, v4, v38, 1.0
	v_lshl_add_u64 v[4:5], v[144:145], 0, s[2:3]
	v_lshlrev_b64 v[42:43], 11, v[4:5]
	v_lshl_add_u64 v[42:43], s[16:17], 0, v[42:43]
	v_lshl_add_u64 v[42:43], v[42:43], 0, s[14:15]
	v_lshl_add_u64 v[42:43], v[142:143], 1, v[42:43]
	v_bfe_u32 v242, v208, 4, 1
	v_mul_u32_u24_e32 v242, 24, v242
	v_mov_b32_e32 v243, 0
	v_lshl_add_u64 v[240:241], v[42:43], 0, v[242:243]
	v_pk_mul_f32 v[236:237], v[98:99], v[40:41] op_sel_hi:[1,0]
	v_pk_mul_f32 v[238:239], v[100:101], v[40:41] op_sel_hi:[1,0]
	v_cvt_pk_bf16_f32 v232, v236, v237
	v_cvt_pk_bf16_f32 v233, v238, v239
	v_pk_mul_f32 v[236:237], v[94:95], v[40:41] op_sel_hi:[1,0]
	v_pk_mul_f32 v[238:239], v[96:97], v[40:41] op_sel_hi:[1,0]
	v_cvt_pk_bf16_f32 v234, v236, v237
	v_cvt_pk_bf16_f32 v235, v238, v239
	s_nop 1
	v_permlane16_swap_b32 v232, v234
	v_permlane16_swap_b32 v233, v235
	global_store_dwordx4 v[240:241], v[232:235], off
	v_pk_mul_f32 v[236:237], v[90:91], v[40:41] op_sel_hi:[1,0]
	v_pk_mul_f32 v[238:239], v[92:93], v[40:41] op_sel_hi:[1,0]
	v_cvt_pk_bf16_f32 v244, v236, v237
	v_cvt_pk_bf16_f32 v245, v238, v239
	v_pk_mul_f32 v[236:237], v[86:87], v[40:41] op_sel_hi:[1,0]
	v_pk_mul_f32 v[238:239], v[88:89], v[40:41] op_sel_hi:[1,0]
	v_cvt_pk_bf16_f32 v246, v236, v237
	v_cvt_pk_bf16_f32 v247, v238, v239
	s_nop 1
	v_permlane16_swap_b32 v244, v246
	v_permlane16_swap_b32 v245, v247
	global_store_dwordx4 v[240:241], v[244:247], off offset:64
	v_pk_mul_f32 v[236:237], v[82:83], v[40:41] op_sel_hi:[1,0]
	v_pk_mul_f32 v[238:239], v[84:85], v[40:41] op_sel_hi:[1,0]
	v_cvt_pk_bf16_f32 v232, v236, v237
	v_cvt_pk_bf16_f32 v233, v238, v239
	v_pk_mul_f32 v[236:237], v[78:79], v[40:41] op_sel_hi:[1,0]
	v_pk_mul_f32 v[238:239], v[80:81], v[40:41] op_sel_hi:[1,0]
	v_cvt_pk_bf16_f32 v234, v236, v237
	v_cvt_pk_bf16_f32 v235, v238, v239
	s_nop 1
	v_permlane16_swap_b32 v232, v234
	v_permlane16_swap_b32 v233, v235
	global_store_dwordx4 v[240:241], v[232:235], off offset:128
	v_pk_mul_f32 v[236:237], v[74:75], v[40:41] op_sel_hi:[1,0]
	v_pk_mul_f32 v[238:239], v[76:77], v[40:41] op_sel_hi:[1,0]
	v_cvt_pk_bf16_f32 v244, v236, v237
	v_cvt_pk_bf16_f32 v245, v238, v239
	v_pk_mul_f32 v[236:237], v[70:71], v[40:41] op_sel_hi:[1,0]
	v_pk_mul_f32 v[238:239], v[72:73], v[40:41] op_sel_hi:[1,0]
	v_cvt_pk_bf16_f32 v246, v236, v237
	v_cvt_pk_bf16_f32 v247, v238, v239
	s_nop 1
	v_permlane16_swap_b32 v244, v246
	v_permlane16_swap_b32 v245, v247
	global_store_dwordx4 v[240:241], v[244:247], off offset:192
	s_and_saveexec_b64 s[44:45], s[0:1]
	s_cbranch_execz .LBB0_408
	v_log_f32_e32 v38, v38
	v_lshlrev_b64 v[4:5], 5, v[4:5]
	v_lshl_add_u64 v[4:5], s[18:19], 0, v[4:5]
	s_lshl_b32 s40, s33, 2
	s_mov_b32 s41, s15
	v_add_f32_e32 v38, v146, v38
	v_lshl_add_u64 v[4:5], v[4:5], 0, s[40:41]
	global_store_dword v[4:5], v38, off
.LBB0_408:
	s_or_b64 exec, exec, s[44:45]
	ds_bpermute_b32 v1, v1, v153
	v_lshl_add_u64 v[4:5], v[140:141], 0, s[2:3]
	v_lshlrev_b64 v[38:39], 11, v[4:5]
	v_lshl_add_u64 v[38:39], s[16:17], 0, v[38:39]
	v_lshl_add_u64 v[38:39], v[38:39], 0, s[14:15]
	s_waitcnt lgkmcnt(0)
	v_add_f32_e32 v1, v153, v1
	ds_bpermute_b32 v3, v3, v1
	v_lshl_add_u64 v[38:39], v[142:143], 1, v[38:39]
	s_waitcnt lgkmcnt(0)
	v_add_f32_e32 v1, v1, v3
	v_div_scale_f32 v3, s[2:3], v1, v1, 1.0
	v_rcp_f32_e32 v40, v3
	v_div_scale_f32 v41, vcc, 1.0, v1, 1.0
	v_fma_f32 v42, -v3, v40, 1.0
	v_fmac_f32_e32 v40, v42, v40
	v_mul_f32_e32 v42, v41, v40
	v_fma_f32 v43, -v3, v42, v41
	v_fmac_f32_e32 v42, v43, v40
	v_fma_f32 v3, -v3, v42, v41
	v_div_fmas_f32 v3, v3, v40, v42
	v_div_fixup_f32 v40, v3, v1, 1.0
	v_lshl_add_u64 v[240:241], v[38:39], 0, v[242:243]
	v_pk_mul_f32 v[236:237], v[34:35], v[40:41] op_sel_hi:[1,0]
	v_pk_mul_f32 v[238:239], v[36:37], v[40:41] op_sel_hi:[1,0]
	v_cvt_pk_bf16_f32 v232, v236, v237
	v_cvt_pk_bf16_f32 v233, v238, v239
	v_pk_mul_f32 v[236:237], v[30:31], v[40:41] op_sel_hi:[1,0]
	v_pk_mul_f32 v[238:239], v[32:33], v[40:41] op_sel_hi:[1,0]
	v_cvt_pk_bf16_f32 v234, v236, v237
	v_cvt_pk_bf16_f32 v235, v238, v239
	s_nop 1
	v_permlane16_swap_b32 v232, v234
	v_permlane16_swap_b32 v233, v235
	global_store_dwordx4 v[240:241], v[232:235], off
	v_pk_mul_f32 v[236:237], v[26:27], v[40:41] op_sel_hi:[1,0]
	v_pk_mul_f32 v[238:239], v[28:29], v[40:41] op_sel_hi:[1,0]
	v_cvt_pk_bf16_f32 v244, v236, v237
	v_cvt_pk_bf16_f32 v245, v238, v239
	v_pk_mul_f32 v[236:237], v[18:19], v[40:41] op_sel_hi:[1,0]
	v_pk_mul_f32 v[238:239], v[20:21], v[40:41] op_sel_hi:[1,0]
	v_cvt_pk_bf16_f32 v246, v236, v237
	v_cvt_pk_bf16_f32 v247, v238, v239
	s_nop 1
	v_permlane16_swap_b32 v244, v246
	v_permlane16_swap_b32 v245, v247
	global_store_dwordx4 v[240:241], v[244:247], off offset:64
	v_pk_mul_f32 v[236:237], v[22:23], v[40:41] op_sel_hi:[1,0]
	v_pk_mul_f32 v[238:239], v[24:25], v[40:41] op_sel_hi:[1,0]
	v_cvt_pk_bf16_f32 v232, v236, v237
	v_cvt_pk_bf16_f32 v233, v238, v239
	v_pk_mul_f32 v[236:237], v[14:15], v[40:41] op_sel_hi:[1,0]
	v_pk_mul_f32 v[238:239], v[16:17], v[40:41] op_sel_hi:[1,0]
	v_cvt_pk_bf16_f32 v234, v236, v237
	v_cvt_pk_bf16_f32 v235, v238, v239
	s_nop 1
	v_permlane16_swap_b32 v232, v234
	v_permlane16_swap_b32 v233, v235
	global_store_dwordx4 v[240:241], v[232:235], off offset:128
	v_pk_mul_f32 v[236:237], v[10:11], v[40:41] op_sel_hi:[1,0]
	v_pk_mul_f32 v[238:239], v[12:13], v[40:41] op_sel_hi:[1,0]
	v_cvt_pk_bf16_f32 v244, v236, v237
	v_cvt_pk_bf16_f32 v245, v238, v239
	v_pk_mul_f32 v[236:237], v[6:7], v[40:41] op_sel_hi:[1,0]
	v_pk_mul_f32 v[238:239], v[8:9], v[40:41] op_sel_hi:[1,0]
	v_cvt_pk_bf16_f32 v246, v236, v237
	v_cvt_pk_bf16_f32 v247, v238, v239
	s_nop 1
	v_permlane16_swap_b32 v244, v246
	v_permlane16_swap_b32 v245, v247
	global_store_dwordx4 v[240:241], v[244:247], off offset:192
	s_and_saveexec_b64 s[2:3], s[0:1]
	s_xor_b64 s[0:1], exec, s[2:3]
	s_cbranch_execz .LBB0_410
	v_log_f32_e32 v1, v1
	v_lshlrev_b64 v[4:5], 5, v[4:5]
	v_lshl_add_u64 v[4:5], s[18:19], 0, v[4:5]
	s_lshl_b32 s14, s33, 2
	v_lshl_add_u64 v[4:5], v[4:5], 0, s[14:15]
	v_add_f32_e32 v1, v2, v1
	global_store_dword v[4:5], v1, off
